# v68 + top-k bisection: compare masks through 4 rotating SGPR pairs issued 4 ahead of their popcounts; passes with candidate above the row max key decided without scan
# speedup vs baseline: 1.0104x; 1.0104x over previous
; __device__ __forceinline__ unsigned fkey(float f) { const unsigned u = __builtin_bit_cast(unsigned, f); return (u & 0x80000000u) ? ~u : (u | 0x80000000u); }
; __device__ __forceinline__ void select_row(Frame& F, int row, int lane_, const LAS float* srl) {
;     ...
;             float sv[32];
; #pragma unroll
;             for (int j = 0; j < 32; ++j) sv[j] = srl[64 * j];
; #pragma unroll
;             for (int j = 0; j < 32; ++j) { const int s = 64 * j + lane; const unsigned fk = fkey(sv[j]); key[j] = (s <= t) ? fk : 0u; }
;         }
;         unsigned long long* mr = F.MASK + (size_t)row * 32;
;         if (t + 1 <= TOPK) {
.LBB0_272:
	s_xor_b64 s[0:1], s[2:3], -1
	v_writelane_b32 v255, s0, 51
	s_waitcnt lgkmcnt(0)
	s_barrier
	v_writelane_b32 v255, s1, 52
	v_readlane_b32 s0, v253, 18
	s_nop 1
	v_xor_b32_e32 v16, s0, v184
	v_readlane_b32 s0, v252, 5
	s_nop 1
	v_lshl_add_u32 v22, v16, 2, s0
	v_mov_b32_e32 v16, v184
	v_readlane_b32 s0, v253, 25
	ds_read2st64_b32 v[24:25], v22 offset1:1
	ds_read2st64_b32 v[26:27], v22 offset0:2 offset1:3
	ds_read2st64_b32 v[28:29], v22 offset0:4 offset1:5
	ds_read2st64_b32 v[30:31], v22 offset0:6 offset1:7
	ds_read2st64_b32 v[32:33], v22 offset0:8 offset1:9
	ds_read2st64_b32 v[34:35], v22 offset0:10 offset1:11
	ds_read2st64_b32 v[36:37], v22 offset0:12 offset1:13
	ds_read2st64_b32 v[38:39], v22 offset0:14 offset1:15
	ds_read2st64_b32 v[40:41], v22 offset0:16 offset1:17
	ds_read2st64_b32 v[42:43], v22 offset0:18 offset1:19
	ds_read2st64_b32 v[44:45], v22 offset0:20 offset1:21
	ds_read2st64_b32 v[46:47], v22 offset0:22 offset1:23
	ds_read2st64_b32 v[48:49], v22 offset0:24 offset1:25
	ds_read2st64_b32 v[50:51], v22 offset0:26 offset1:27
	ds_read2st64_b32 v[20:21], v22 offset0:28 offset1:29
	ds_read2st64_b32 v[18:19], v22 offset0:30 offset1:31
	s_waitcnt lgkmcnt(14)
	v_and_b32_e32 v53, 0x7fffffff, v24
	v_and_b32_e32 v52, 0x7fffffff, v25
	s_add_i32 s10, s6, s0
	v_xor_b32_e32 v54, -1, v25
	v_pk_add_f32 v[52:53], v[52:53], 0 neg_lo:[1,1] neg_hi:[1,1]
	v_cmp_gt_i32_e32 vcc, 0, v25
	s_and_b32 s2, s10, 0x7fe
	v_xor_b32_e32 v17, -1, v24
	v_cndmask_b32_e32 v25, v52, v54, vcc
	v_cmp_gt_i32_e32 vcc, 0, v24
	v_add_u32_e32 v23, 64, v16
	v_and_b32_e32 v24, 0x7fffffff, v27
	v_cndmask_b32_e32 v17, v53, v17, vcc
	v_cmp_ge_i32_e32 vcc, s2, v16
	v_xor_b32_e32 v55, -1, v27
	v_add_u32_e32 v53, 0x80, v16
	v_cndmask_b32_e32 v17, 0, v17, vcc
	v_cmp_ge_i32_e32 vcc, s2, v23
	v_xor_b32_e32 v54, -1, v26
	v_add_u32_e32 v52, 0xc0, v16
	v_cndmask_b32_e32 v23, 0, v25, vcc
	v_and_b32_e32 v25, 0x7fffffff, v26
	v_pk_add_f32 v[24:25], v[24:25], 0 neg_lo:[1,1] neg_hi:[1,1]
	v_cmp_gt_i32_e32 vcc, 0, v27
	s_cmpk_gt_u32 s2, 0xff
	s_nop 0
	v_cndmask_b32_e32 v27, v24, v55, vcc
	v_cmp_gt_i32_e32 vcc, 0, v26
	s_waitcnt lgkmcnt(13)
	v_and_b32_e32 v26, 0x7fffffff, v29
	v_xor_b32_e32 v55, -1, v29
	v_cndmask_b32_e32 v24, v25, v54, vcc
	v_cmp_ge_i32_e32 vcc, s2, v53
	v_add_u32_e32 v53, 0x100, v16
	v_xor_b32_e32 v54, -1, v28
	v_cndmask_b32_e32 v24, 0, v24, vcc
	v_cmp_ge_i32_e32 vcc, s2, v52
	v_add_u32_e32 v52, 0x140, v16
	s_nop 0
	v_cndmask_b32_e32 v25, 0, v27, vcc
	v_and_b32_e32 v27, 0x7fffffff, v28
	v_pk_add_f32 v[26:27], v[26:27], 0 neg_lo:[1,1] neg_hi:[1,1]
	v_cmp_gt_i32_e32 vcc, 0, v29
	s_nop 1
	v_cndmask_b32_e32 v29, v26, v55, vcc
	v_cmp_gt_i32_e32 vcc, 0, v28
	s_waitcnt lgkmcnt(12)
	v_and_b32_e32 v28, 0x7fffffff, v31
	v_xor_b32_e32 v55, -1, v31
	v_cndmask_b32_e32 v26, v27, v54, vcc
	v_cmp_ge_i32_e32 vcc, s2, v53
	v_add_u32_e32 v53, 0x180, v16
	v_xor_b32_e32 v54, -1, v30
	v_cndmask_b32_e32 v26, 0, v26, vcc
	v_cmp_ge_i32_e32 vcc, s2, v52
	v_add_u32_e32 v52, 0x1c0, v16
	s_nop 0
	v_cndmask_b32_e32 v27, 0, v29, vcc
	v_and_b32_e32 v29, 0x7fffffff, v30
	v_pk_add_f32 v[28:29], v[28:29], 0 neg_lo:[1,1] neg_hi:[1,1]
	v_cmp_gt_i32_e32 vcc, 0, v31
	s_nop 1
	v_cndmask_b32_e32 v31, v28, v55, vcc
	v_cmp_gt_i32_e32 vcc, 0, v30
	s_waitcnt lgkmcnt(11)
	v_and_b32_e32 v30, 0x7fffffff, v33
	v_xor_b32_e32 v55, -1, v33
	v_cndmask_b32_e32 v28, v29, v54, vcc
	v_cmp_ge_i32_e32 vcc, s2, v53
	v_add_u32_e32 v53, 0x200, v16
	v_xor_b32_e32 v54, -1, v32
	v_cndmask_b32_e32 v28, 0, v28, vcc
	v_cmp_ge_i32_e32 vcc, s2, v52
	v_add_u32_e32 v52, 0x240, v16
	s_nop 0
	v_cndmask_b32_e32 v29, 0, v31, vcc
	v_and_b32_e32 v31, 0x7fffffff, v32
	v_pk_add_f32 v[30:31], v[30:31], 0 neg_lo:[1,1] neg_hi:[1,1]
	v_cmp_gt_i32_e32 vcc, 0, v33
	s_nop 1
	v_cndmask_b32_e32 v33, v30, v55, vcc
	v_cmp_gt_i32_e32 vcc, 0, v32
	s_waitcnt lgkmcnt(10)
	v_and_b32_e32 v32, 0x7fffffff, v35
	v_xor_b32_e32 v55, -1, v35
	v_cndmask_b32_e32 v30, v31, v54, vcc
	v_cmp_ge_i32_e32 vcc, s2, v53
	v_add_u32_e32 v53, 0x280, v16
	v_xor_b32_e32 v54, -1, v34
	v_cndmask_b32_e32 v30, 0, v30, vcc
	v_cmp_ge_i32_e32 vcc, s2, v52
	v_add_u32_e32 v52, 0x2c0, v16
	s_nop 0
	v_cndmask_b32_e32 v31, 0, v33, vcc
	v_and_b32_e32 v33, 0x7fffffff, v34
	v_pk_add_f32 v[32:33], v[32:33], 0 neg_lo:[1,1] neg_hi:[1,1]
	v_cmp_gt_i32_e32 vcc, 0, v35
	s_nop 1
	v_cndmask_b32_e32 v35, v32, v55, vcc
	v_cmp_gt_i32_e32 vcc, 0, v34
	s_waitcnt lgkmcnt(9)
	v_and_b32_e32 v34, 0x7fffffff, v37
	v_xor_b32_e32 v55, -1, v37
	v_cndmask_b32_e32 v32, v33, v54, vcc
	v_cmp_ge_i32_e32 vcc, s2, v53
	v_add_u32_e32 v53, 0x300, v16
	v_xor_b32_e32 v54, -1, v36
	v_cndmask_b32_e32 v32, 0, v32, vcc
	v_cmp_ge_i32_e32 vcc, s2, v52
	v_add_u32_e32 v52, 0x340, v16
	s_nop 0
	v_cndmask_b32_e32 v33, 0, v35, vcc
	v_and_b32_e32 v35, 0x7fffffff, v36
	v_pk_add_f32 v[34:35], v[34:35], 0 neg_lo:[1,1] neg_hi:[1,1]
	v_cmp_gt_i32_e32 vcc, 0, v37
	s_nop 1
	v_cndmask_b32_e32 v37, v34, v55, vcc
	v_cmp_gt_i32_e32 vcc, 0, v36
	s_waitcnt lgkmcnt(8)
	v_and_b32_e32 v36, 0x7fffffff, v39
	v_xor_b32_e32 v55, -1, v39
	v_cndmask_b32_e32 v34, v35, v54, vcc
	v_cmp_ge_i32_e32 vcc, s2, v53
	v_add_u32_e32 v53, 0x380, v16
	v_xor_b32_e32 v54, -1, v38
	v_cndmask_b32_e32 v34, 0, v34, vcc
	v_cmp_ge_i32_e32 vcc, s2, v52
	v_add_u32_e32 v52, 0x3c0, v16
	s_nop 0
	v_cndmask_b32_e32 v35, 0, v37, vcc
	v_and_b32_e32 v37, 0x7fffffff, v38
	v_pk_add_f32 v[36:37], v[36:37], 0 neg_lo:[1,1] neg_hi:[1,1]
	v_cmp_gt_i32_e32 vcc, 0, v39
	s_nop 1
	v_cndmask_b32_e32 v39, v36, v55, vcc
	v_cmp_gt_i32_e32 vcc, 0, v38
	s_waitcnt lgkmcnt(7)
; __device__ __forceinline__ unsigned fkey(float f) { const unsigned u = __builtin_bit_cast(unsigned, f); return (u & 0x80000000u) ? ~u : (u | 0x80000000u); }
; __device__ __forceinline__ void select_row(Frame& F, int row, int lane_, const LAS float* srl) {
;     ...
;             for (int j = 0; j < 32; ++j) { const int s = 64 * j + lane; const unsigned fk = fkey(sv[j]); key[j] = (s <= t) ? fk : 0u; }
;         }
;         unsigned long long* mr = F.MASK + (size_t)row * 32;
;         if (t + 1 <= TOPK) {
;             unsigned long long mine = 0ull;
; #pragma unroll
;             for (int j = 0; j < 32; ++j) { const unsigned long long bm = __ballot(key[j] != 0u); mine = (lane == j) ? bm : mine; }
;             if (lane < 32) mr[lane] = mine;
;             return;
;         }
;         unsigned T = 0u; bool exact = false;
;         const int nj = __builtin_amdgcn_readfirstlane((t + 64) >> 6);
;         int clo = t + 1, chi = 0, bit = 31;
;     ...
;             if (clo - chi <= 64) break;
;             const unsigned cand = T | (1u << bit);
;             int c = cnt_ge<0, 8>(key, cand);
;             if (nj > 8) { c += cnt_ge<8, 16>(key, cand); if (nj > 16) { c += cnt_ge<16, 24>(key, cand); if (nj > 24) c += cnt_ge<24, 32>(key, cand); } }
	v_and_b32_e32 v38, 0x7fffffff, v41
	v_xor_b32_e32 v55, -1, v41
	v_cndmask_b32_e32 v36, v37, v54, vcc
	v_cmp_ge_i32_e32 vcc, s2, v53
	v_add_u32_e32 v53, 0x400, v16
	v_xor_b32_e32 v54, -1, v40
	v_cndmask_b32_e32 v36, 0, v36, vcc
	v_cmp_ge_i32_e32 vcc, s2, v52
	v_add_u32_e32 v52, 0x440, v16
	s_nop 0
	v_cndmask_b32_e32 v37, 0, v39, vcc
	v_and_b32_e32 v39, 0x7fffffff, v40
	v_pk_add_f32 v[38:39], v[38:39], 0 neg_lo:[1,1] neg_hi:[1,1]
	v_cmp_gt_i32_e32 vcc, 0, v41
	s_nop 1
	v_cndmask_b32_e32 v41, v38, v55, vcc
	v_cmp_gt_i32_e32 vcc, 0, v40
	s_waitcnt lgkmcnt(6)
	v_and_b32_e32 v40, 0x7fffffff, v43
	v_xor_b32_e32 v55, -1, v43
	v_cndmask_b32_e32 v38, v39, v54, vcc
	v_cmp_ge_i32_e32 vcc, s2, v53
	v_add_u32_e32 v53, 0x480, v16
	v_xor_b32_e32 v54, -1, v42
	v_cndmask_b32_e32 v38, 0, v38, vcc
	v_cmp_ge_i32_e32 vcc, s2, v52
	v_add_u32_e32 v52, 0x4c0, v16
	s_nop 0
	v_cndmask_b32_e32 v39, 0, v41, vcc
	v_and_b32_e32 v41, 0x7fffffff, v42
	v_pk_add_f32 v[40:41], v[40:41], 0 neg_lo:[1,1] neg_hi:[1,1]
	v_cmp_gt_i32_e32 vcc, 0, v43
	s_nop 1
	v_cndmask_b32_e32 v43, v40, v55, vcc
	v_cmp_gt_i32_e32 vcc, 0, v42
	s_waitcnt lgkmcnt(5)
	v_and_b32_e32 v42, 0x7fffffff, v45
	v_xor_b32_e32 v55, -1, v45
	v_cndmask_b32_e32 v40, v41, v54, vcc
	v_cmp_ge_i32_e32 vcc, s2, v53
	v_add_u32_e32 v53, 0x500, v16
	v_xor_b32_e32 v54, -1, v44
	v_cndmask_b32_e32 v40, 0, v40, vcc
	v_cmp_ge_i32_e32 vcc, s2, v52
	v_add_u32_e32 v52, 0x540, v16
	s_nop 0
	v_cndmask_b32_e32 v41, 0, v43, vcc
	v_and_b32_e32 v43, 0x7fffffff, v44
	v_pk_add_f32 v[42:43], v[42:43], 0 neg_lo:[1,1] neg_hi:[1,1]
	v_cmp_gt_i32_e32 vcc, 0, v45
	s_nop 1
	v_cndmask_b32_e32 v45, v42, v55, vcc
	v_cmp_gt_i32_e32 vcc, 0, v44
	s_waitcnt lgkmcnt(4)
	v_and_b32_e32 v44, 0x7fffffff, v47
	v_xor_b32_e32 v55, -1, v47
	v_cndmask_b32_e32 v42, v43, v54, vcc
	v_cmp_ge_i32_e32 vcc, s2, v53
	v_add_u32_e32 v53, 0x580, v16
	v_xor_b32_e32 v54, -1, v46
	v_cndmask_b32_e32 v42, 0, v42, vcc
	v_cmp_ge_i32_e32 vcc, s2, v52
	v_add_u32_e32 v52, 0x5c0, v16
	s_nop 0
	v_cndmask_b32_e32 v43, 0, v45, vcc
	v_and_b32_e32 v45, 0x7fffffff, v46
	v_pk_add_f32 v[44:45], v[44:45], 0 neg_lo:[1,1] neg_hi:[1,1]
	v_cmp_gt_i32_e32 vcc, 0, v47
	s_nop 1
	v_cndmask_b32_e32 v47, v44, v55, vcc
	v_cmp_gt_i32_e32 vcc, 0, v46
	s_waitcnt lgkmcnt(3)
	v_and_b32_e32 v46, 0x7fffffff, v49
	v_xor_b32_e32 v55, -1, v49
	v_cndmask_b32_e32 v44, v45, v54, vcc
	v_cmp_ge_i32_e32 vcc, s2, v53
	v_add_u32_e32 v53, 0x600, v16
	v_xor_b32_e32 v54, -1, v48
	v_cndmask_b32_e32 v44, 0, v44, vcc
	v_cmp_ge_i32_e32 vcc, s2, v52
	v_add_u32_e32 v52, 0x640, v16
	s_nop 0
	v_cndmask_b32_e32 v45, 0, v47, vcc
	v_and_b32_e32 v47, 0x7fffffff, v48
	v_pk_add_f32 v[46:47], v[46:47], 0 neg_lo:[1,1] neg_hi:[1,1]
	v_cmp_gt_i32_e32 vcc, 0, v49
	s_nop 1
	v_cndmask_b32_e32 v49, v46, v55, vcc
	v_cmp_gt_i32_e32 vcc, 0, v48
	s_waitcnt lgkmcnt(2)
	v_and_b32_e32 v48, 0x7fffffff, v51
	v_xor_b32_e32 v55, -1, v51
	v_cndmask_b32_e32 v46, v47, v54, vcc
	v_cmp_ge_i32_e32 vcc, s2, v53
	v_add_u32_e32 v53, 0x680, v16
	v_xor_b32_e32 v54, -1, v50
	v_cndmask_b32_e32 v46, 0, v46, vcc
	v_cmp_ge_i32_e32 vcc, s2, v52
	v_add_u32_e32 v52, 0x6c0, v16
	s_nop 0
	v_cndmask_b32_e32 v47, 0, v49, vcc
	v_and_b32_e32 v49, 0x7fffffff, v50
	v_pk_add_f32 v[48:49], v[48:49], 0 neg_lo:[1,1] neg_hi:[1,1]
	v_cmp_gt_i32_e32 vcc, 0, v51
	s_nop 1
	v_cndmask_b32_e32 v51, v48, v55, vcc
	v_cmp_gt_i32_e32 vcc, 0, v50
	s_waitcnt lgkmcnt(1)
	v_and_b32_e32 v50, 0x7fffffff, v21
	v_xor_b32_e32 v55, -1, v21
	v_cndmask_b32_e32 v48, v49, v54, vcc
	v_cmp_ge_i32_e32 vcc, s2, v53
	v_add_u32_e32 v53, 0x700, v16
	v_xor_b32_e32 v54, -1, v20
	v_cndmask_b32_e32 v48, 0, v48, vcc
	v_cmp_ge_i32_e32 vcc, s2, v52
	v_add_u32_e32 v52, 0x740, v16
	s_nop 0
	v_cndmask_b32_e32 v49, 0, v51, vcc
	v_and_b32_e32 v51, 0x7fffffff, v20
	v_pk_add_f32 v[50:51], v[50:51], 0 neg_lo:[1,1] neg_hi:[1,1]
	v_cmp_gt_i32_e32 vcc, 0, v21
	s_nop 1
	v_cndmask_b32_e32 v21, v50, v55, vcc
	v_cmp_gt_i32_e32 vcc, 0, v20
	s_waitcnt lgkmcnt(0)
	v_and_b32_e32 v50, 0x7fffffff, v19
	v_xor_b32_e32 v55, -1, v19
	v_cndmask_b32_e32 v20, v51, v54, vcc
	v_cmp_ge_i32_e32 vcc, s2, v53
	v_and_b32_e32 v51, 0x7fffffff, v18
	v_pk_add_f32 v[50:51], v[50:51], 0 neg_lo:[1,1] neg_hi:[1,1]
	v_cndmask_b32_e32 v20, 0, v20, vcc
	v_cmp_ge_i32_e32 vcc, s2, v52
	v_add_u32_e32 v53, 0x780, v16
	v_xor_b32_e32 v54, -1, v18
	v_cndmask_b32_e32 v21, 0, v21, vcc
	v_cmp_gt_i32_e32 vcc, 0, v19
	v_add_u32_e32 v52, 0x7c0, v16
	s_nop 0
	v_cndmask_b32_e32 v19, v50, v55, vcc
	v_cmp_gt_i32_e32 vcc, 0, v18
	s_nop 1
	v_cndmask_b32_e32 v18, v51, v54, vcc
	v_cmp_ge_i32_e32 vcc, s2, v53
	s_nop 1
	v_cndmask_b32_e32 v50, 0, v18, vcc
	v_cmp_ge_i32_e32 vcc, s2, v52
	s_nop 1
	v_cndmask_b32_e32 v51, 0, v19, vcc
	s_cbranch_scc0 .LBB0_286
	s_or_b32 s23, s2, 1
	s_cmpk_gt_u32 s2, 0x1ff
	s_cselect_b64 s[4:5], -1, 0
	s_cmpk_gt_u32 s2, 0x3ff
	s_cselect_b64 s[16:17], -1, 0
	s_cmpk_gt_u32 s2, 0x5ff
	s_mov_b64 s[0:1], s[72:73]
	s_cselect_b64 s[72:73], -1, 0
	s_mov_b32 s18, 31
	s_mov_b64 s[2:3], 0
	s_mov_b32 s20, 0
	s_mov_b32 s13, 0
	v_max3_u32 v18, v17, v23, v24
	v_max3_u32 v18, v18, v25, v26
	v_max3_u32 v18, v18, v27, v28
	v_max3_u32 v18, v18, v29, v30
	v_max3_u32 v18, v18, v31, v32
	v_max3_u32 v18, v18, v33, v34
	v_max3_u32 v18, v18, v35, v36
	v_max3_u32 v18, v18, v37, v38
	v_max3_u32 v18, v18, v39, v40
	v_max3_u32 v18, v18, v41, v42
	v_max3_u32 v18, v18, v43, v44
	v_max3_u32 v18, v18, v45, v46
	v_max3_u32 v18, v18, v47, v48
	v_max3_u32 v18, v18, v49, v20
	v_max3_u32 v18, v18, v21, v50
	v_max_u32_e32 v18, v18, v51
	s_nop 1
	v_max_u32_dpp v18, v18, v18 quad_perm:[1,0,3,2] row_mask:0xf bank_mask:0xf
	s_nop 1
	v_max_u32_dpp v18, v18, v18 quad_perm:[2,3,0,1] row_mask:0xf bank_mask:0xf
	s_nop 1
	v_max_u32_dpp v18, v18, v18 row_half_mirror row_mask:0xf bank_mask:0xf
	s_nop 1
	v_max_u32_dpp v18, v18, v18 row_mirror row_mask:0xf bank_mask:0xf
	s_nop 1
	v_readlane_b32 s6, v18, 0
	v_readlane_b32 s7, v18, 16
	v_readlane_b32 s39, v18, 32
	v_readlane_b32 s40, v18, 48
	s_max_u32 s6, s6, s7
	s_max_u32 s39, s39, s40
	s_max_u32 s101, s6, s39
; template <int J0, int J1> __device__ __forceinline__ int cnt_ge(const unsigned (&key)[32], unsigned cand) {
;     int c = 0;
; #pragma unroll
;     for (int j = J0; j < J1; ++j) c += __popcll(__ballot(key[j] >= cand));
;     return c;
; }
; __device__ __forceinline__ void select_row(Frame& F, int row, int lane_, const LAS float* srl) {
;     ...
;             if (clo - chi <= 64) break;
;             const unsigned cand = T | (1u << bit);
;             int c = cnt_ge<0, 8>(key, cand);
;             if (nj > 8) { c += cnt_ge<8, 16>(key, cand); if (nj > 16) { c += cnt_ge<16, 24>(key, cand); if (nj > 24) c += cnt_ge<24, 32>(key, cand); } }
;             if (c >= TOPK) { T = cand; clo = c; if (c == TOPK) { exact = true; break; } } else chi = c;
.LBB0_274:
	s_lshl_b32 s6, 1, s18
	s_or_b32 s22, s6, s20
	s_cmp_gt_u32 s22, s101
	s_cbranch_scc1 .Lsel1_none
	v_cmp_le_u32_e64 s[44:45], s22, v17
	v_cmp_le_u32_e64 s[46:47], s22, v23
	v_cmp_le_u32_e64 s[48:49], s22, v24
	v_cmp_le_u32_e64 s[50:51], s22, v25
	s_bcnt1_i32_b64 s6, s[44:45]
	v_cmp_le_u32_e64 s[44:45], s22, v26
	s_bcnt1_i32_b64 s7, s[46:47]
	v_cmp_le_u32_e64 s[46:47], s22, v27
	s_add_i32 s6, s6, s7
	s_bcnt1_i32_b64 s7, s[48:49]
	v_cmp_le_u32_e64 s[48:49], s22, v28
	s_add_i32 s6, s6, s7
	s_bcnt1_i32_b64 s7, s[50:51]
	v_cmp_le_u32_e64 s[50:51], s22, v29
	s_add_i32 s6, s6, s7
	s_bcnt1_i32_b64 s7, s[44:45]
	s_add_i32 s6, s6, s7
	s_bcnt1_i32_b64 s7, s[46:47]
	s_add_i32 s6, s6, s7
	s_bcnt1_i32_b64 s7, s[48:49]
	s_add_i32 s6, s6, s7
	s_bcnt1_i32_b64 s7, s[50:51]
	s_add_i32 s38, s6, s7
	v_cndmask_b32_e64 v18, 0, 1, s[4:5]
	v_cmp_ne_u32_e64 s[36:37], 1, v18
	s_andn2_b64 vcc, exec, s[4:5]
	s_cbranch_vccnz .LBB0_278
	v_cmp_le_u32_e64 s[44:45], s22, v30
	v_cmp_le_u32_e64 s[46:47], s22, v31
	v_cmp_le_u32_e64 s[48:49], s22, v32
	v_cmp_le_u32_e64 s[50:51], s22, v33
	s_bcnt1_i32_b64 s7, s[44:45]
	v_cmp_le_u32_e64 s[44:45], s22, v34
	s_add_i32 s6, s38, s7
	s_bcnt1_i32_b64 s7, s[46:47]
	v_cmp_le_u32_e64 s[46:47], s22, v35
	s_add_i32 s6, s6, s7
	s_bcnt1_i32_b64 s7, s[48:49]
	v_cmp_le_u32_e64 s[48:49], s22, v36
	s_add_i32 s6, s6, s7
	s_bcnt1_i32_b64 s7, s[50:51]
	v_cmp_le_u32_e64 s[50:51], s22, v37
	s_add_i32 s6, s6, s7
	s_bcnt1_i32_b64 s7, s[44:45]
	s_add_i32 s6, s6, s7
	s_bcnt1_i32_b64 s7, s[46:47]
	s_add_i32 s6, s6, s7
	s_bcnt1_i32_b64 s7, s[48:49]
	s_add_i32 s6, s6, s7
	s_bcnt1_i32_b64 s7, s[50:51]
	s_add_i32 s38, s6, s7
	s_andn2_b64 vcc, exec, s[16:17]
	s_cbranch_vccnz .LBB0_278
	v_cmp_le_u32_e64 s[44:45], s22, v38
	v_cmp_le_u32_e64 s[46:47], s22, v39
	v_cmp_le_u32_e64 s[48:49], s22, v40
	v_cmp_le_u32_e64 s[50:51], s22, v41
	s_bcnt1_i32_b64 s7, s[44:45]
	v_cmp_le_u32_e64 s[44:45], s22, v42
	s_add_i32 s6, s38, s7
	s_bcnt1_i32_b64 s7, s[46:47]
	v_cmp_le_u32_e64 s[46:47], s22, v43
	s_add_i32 s6, s6, s7
	s_bcnt1_i32_b64 s7, s[48:49]
	v_cmp_le_u32_e64 s[48:49], s22, v44
	s_add_i32 s6, s6, s7
	s_bcnt1_i32_b64 s7, s[50:51]
	v_cmp_le_u32_e64 s[50:51], s22, v45
	s_add_i32 s6, s6, s7
	s_bcnt1_i32_b64 s7, s[44:45]
	s_add_i32 s6, s6, s7
	s_bcnt1_i32_b64 s7, s[46:47]
	s_add_i32 s6, s6, s7
	s_bcnt1_i32_b64 s7, s[48:49]
	s_add_i32 s6, s6, s7
	s_bcnt1_i32_b64 s7, s[50:51]
	s_add_i32 s38, s6, s7
	s_andn2_b64 vcc, exec, s[72:73]
	s_cbranch_vccnz .LBB0_278
	v_cmp_le_u32_e64 s[44:45], s22, v46
	v_cmp_le_u32_e64 s[46:47], s22, v47
	v_cmp_le_u32_e64 s[48:49], s22, v48
	v_cmp_le_u32_e64 s[50:51], s22, v49
	s_bcnt1_i32_b64 s7, s[44:45]
	v_cmp_le_u32_e64 s[44:45], s22, v20
	s_add_i32 s6, s38, s7
	s_bcnt1_i32_b64 s7, s[46:47]
	v_cmp_le_u32_e64 s[46:47], s22, v21
	s_add_i32 s6, s6, s7
	s_bcnt1_i32_b64 s7, s[48:49]
	v_cmp_le_u32_e64 s[48:49], s22, v50
	s_add_i32 s6, s6, s7
	s_bcnt1_i32_b64 s7, s[50:51]
	v_cmp_le_u32_e64 s[50:51], s22, v51
	s_add_i32 s6, s6, s7
	s_bcnt1_i32_b64 s7, s[44:45]
	s_add_i32 s6, s6, s7
	s_bcnt1_i32_b64 s7, s[46:47]
	s_add_i32 s6, s6, s7
	s_bcnt1_i32_b64 s7, s[48:49]
	s_add_i32 s6, s6, s7
	s_bcnt1_i32_b64 s7, s[50:51]
	s_add_i32 s38, s6, s7

; __device__ __forceinline__ void select_row(Frame& F, int row, int lane_, const LAS float* srl) {
;     ...
;             if (c >= TOPK) { T = cand; clo = c; if (c == TOPK) { exact = true; break; } } else chi = c;
.Lsel1_none:
	s_andn2_b64 s[36:37], exec, s[4:5]
	s_mov_b32 s38, 0
	s_branch .LBB0_278

; __device__ __forceinline__ unsigned fkey(float f) { const unsigned u = __builtin_bit_cast(unsigned, f); return (u & 0x80000000u) ? ~u : (u | 0x80000000u); }
; __device__ __forceinline__ void select_row(Frame& F, int row, int lane_, const LAS float* srl) {
;     ...
;             float sv[32];
; #pragma unroll
;             for (int j = 0; j < 32; ++j) sv[j] = srl[64 * j];
; #pragma unroll
;             for (int j = 0; j < 32; ++j) { const int s = 64 * j + lane; const unsigned fk = fkey(sv[j]); key[j] = (s <= t) ? fk : 0u; }
.LBB0_379:
	s_or_b64 exec, exec, s[2:3]
	ds_read2st64_b32 v[20:21], v22 offset0:32 offset1:33
	ds_read2st64_b32 v[24:25], v22 offset0:34 offset1:35
	ds_read2st64_b32 v[26:27], v22 offset0:36 offset1:37
	ds_read2st64_b32 v[28:29], v22 offset0:38 offset1:39
	ds_read2st64_b32 v[30:31], v22 offset0:40 offset1:41
	ds_read2st64_b32 v[32:33], v22 offset0:42 offset1:43
	ds_read2st64_b32 v[34:35], v22 offset0:44 offset1:45
	ds_read2st64_b32 v[36:37], v22 offset0:46 offset1:47
	ds_read2st64_b32 v[38:39], v22 offset0:48 offset1:49
	ds_read2st64_b32 v[40:41], v22 offset0:50 offset1:51
	ds_read2st64_b32 v[42:43], v22 offset0:52 offset1:53
	ds_read2st64_b32 v[44:45], v22 offset0:54 offset1:55
	ds_read2st64_b32 v[46:47], v22 offset0:56 offset1:57
	ds_read2st64_b32 v[48:49], v22 offset0:58 offset1:59
	ds_read2st64_b32 v[18:19], v22 offset0:60 offset1:61
	ds_read2st64_b32 v[16:17], v22 offset0:62 offset1:63
	s_waitcnt lgkmcnt(14)
	v_and_b32_e32 v23, 0x7fffffff, v20
	v_and_b32_e32 v22, 0x7fffffff, v21
	s_or_b32 s0, s10, 1
	v_xor_b32_e32 v52, -1, v21
	v_pk_add_f32 v[22:23], v[22:23], 0 neg_lo:[1,1] neg_hi:[1,1]
	v_cmp_gt_i32_e32 vcc, 0, v21
	s_and_b32 s2, s0, 0x7ff
	v_xor_b32_e32 v51, -1, v20
	v_cndmask_b32_e32 v21, v22, v52, vcc
	v_cmp_gt_i32_e32 vcc, 0, v20
	v_add_u32_e32 v50, 64, v184
	v_and_b32_e32 v22, 0x7fffffff, v25
	v_cndmask_b32_e32 v20, v23, v51, vcc
	v_cmp_ge_i32_e32 vcc, s2, v184
	v_and_b32_e32 v23, 0x7fffffff, v24
	v_xor_b32_e32 v53, -1, v25
	v_cndmask_b32_e32 v20, 0, v20, vcc
	v_cmp_ge_i32_e32 vcc, s2, v50
	v_pk_add_f32 v[22:23], v[22:23], 0 neg_lo:[1,1] neg_hi:[1,1]
	v_add_u32_e32 v51, 0x80, v184
	v_cndmask_b32_e32 v21, 0, v21, vcc
	v_cmp_gt_i32_e32 vcc, 0, v25
	v_xor_b32_e32 v52, -1, v24
	v_add_u32_e32 v50, 0xc0, v184
	v_cndmask_b32_e32 v25, v22, v53, vcc
	v_cmp_gt_i32_e32 vcc, 0, v24
	s_waitcnt lgkmcnt(13)
	v_and_b32_e32 v24, 0x7fffffff, v27
	v_xor_b32_e32 v53, -1, v27
	v_cndmask_b32_e32 v22, v23, v52, vcc
	v_cmp_ge_i32_e32 vcc, s2, v51
	v_add_u32_e32 v51, 0x100, v184
	v_xor_b32_e32 v52, -1, v26
	v_cndmask_b32_e32 v22, 0, v22, vcc
	v_cmp_ge_i32_e32 vcc, s2, v50
	v_add_u32_e32 v50, 0x140, v184
	s_cmpk_gt_u32 s2, 0xff
	v_cndmask_b32_e32 v23, 0, v25, vcc
	v_and_b32_e32 v25, 0x7fffffff, v26
	v_pk_add_f32 v[24:25], v[24:25], 0 neg_lo:[1,1] neg_hi:[1,1]
	v_cmp_gt_i32_e32 vcc, 0, v27
	s_nop 1
	v_cndmask_b32_e32 v27, v24, v53, vcc
	v_cmp_gt_i32_e32 vcc, 0, v26
	s_waitcnt lgkmcnt(12)
	v_and_b32_e32 v26, 0x7fffffff, v29
	v_xor_b32_e32 v53, -1, v29
	v_cndmask_b32_e32 v24, v25, v52, vcc
	v_cmp_ge_i32_e32 vcc, s2, v51
	v_add_u32_e32 v51, 0x180, v184
	v_xor_b32_e32 v52, -1, v28
	v_cndmask_b32_e32 v24, 0, v24, vcc
	v_cmp_ge_i32_e32 vcc, s2, v50
	v_add_u32_e32 v50, 0x1c0, v184
	s_nop 0
	v_cndmask_b32_e32 v25, 0, v27, vcc
	v_and_b32_e32 v27, 0x7fffffff, v28
	v_pk_add_f32 v[26:27], v[26:27], 0 neg_lo:[1,1] neg_hi:[1,1]
	v_cmp_gt_i32_e32 vcc, 0, v29
	s_nop 1
	v_cndmask_b32_e32 v29, v26, v53, vcc
	v_cmp_gt_i32_e32 vcc, 0, v28
	s_waitcnt lgkmcnt(11)
	v_and_b32_e32 v28, 0x7fffffff, v31
	v_xor_b32_e32 v53, -1, v31
	v_cndmask_b32_e32 v26, v27, v52, vcc
	v_cmp_ge_i32_e32 vcc, s2, v51
	v_add_u32_e32 v51, 0x200, v184
	v_xor_b32_e32 v52, -1, v30
	v_cndmask_b32_e32 v26, 0, v26, vcc
	v_cmp_ge_i32_e32 vcc, s2, v50
	v_add_u32_e32 v50, 0x240, v184
	s_nop 0
	v_cndmask_b32_e32 v27, 0, v29, vcc
	v_and_b32_e32 v29, 0x7fffffff, v30
	v_pk_add_f32 v[28:29], v[28:29], 0 neg_lo:[1,1] neg_hi:[1,1]
	v_cmp_gt_i32_e32 vcc, 0, v31
	s_nop 1
	v_cndmask_b32_e32 v31, v28, v53, vcc
	v_cmp_gt_i32_e32 vcc, 0, v30
	s_waitcnt lgkmcnt(10)
	v_and_b32_e32 v30, 0x7fffffff, v33
	v_xor_b32_e32 v53, -1, v33
	v_cndmask_b32_e32 v28, v29, v52, vcc
	v_cmp_ge_i32_e32 vcc, s2, v51
	v_add_u32_e32 v51, 0x280, v184
	v_xor_b32_e32 v52, -1, v32
	v_cndmask_b32_e32 v28, 0, v28, vcc
	v_cmp_ge_i32_e32 vcc, s2, v50
	v_add_u32_e32 v50, 0x2c0, v184
	s_nop 0
	v_cndmask_b32_e32 v29, 0, v31, vcc
	v_and_b32_e32 v31, 0x7fffffff, v32
	v_pk_add_f32 v[30:31], v[30:31], 0 neg_lo:[1,1] neg_hi:[1,1]
	v_cmp_gt_i32_e32 vcc, 0, v33
	s_nop 1
	v_cndmask_b32_e32 v33, v30, v53, vcc
	v_cmp_gt_i32_e32 vcc, 0, v32
	s_waitcnt lgkmcnt(9)
	v_and_b32_e32 v32, 0x7fffffff, v35
	v_xor_b32_e32 v53, -1, v35
	v_cndmask_b32_e32 v30, v31, v52, vcc
	v_cmp_ge_i32_e32 vcc, s2, v51
	v_add_u32_e32 v51, 0x300, v184
	v_xor_b32_e32 v52, -1, v34
	v_cndmask_b32_e32 v30, 0, v30, vcc
	v_cmp_ge_i32_e32 vcc, s2, v50
	v_add_u32_e32 v50, 0x340, v184
	s_nop 0
	v_cndmask_b32_e32 v31, 0, v33, vcc
	v_and_b32_e32 v33, 0x7fffffff, v34
	v_pk_add_f32 v[32:33], v[32:33], 0 neg_lo:[1,1] neg_hi:[1,1]
	v_cmp_gt_i32_e32 vcc, 0, v35
	s_nop 1
	v_cndmask_b32_e32 v35, v32, v53, vcc
	v_cmp_gt_i32_e32 vcc, 0, v34
	s_waitcnt lgkmcnt(8)
	v_and_b32_e32 v34, 0x7fffffff, v37
	v_xor_b32_e32 v53, -1, v37
	v_cndmask_b32_e32 v32, v33, v52, vcc
	v_cmp_ge_i32_e32 vcc, s2, v51
	v_add_u32_e32 v51, 0x380, v184
	v_xor_b32_e32 v52, -1, v36
	v_cndmask_b32_e32 v32, 0, v32, vcc
	v_cmp_ge_i32_e32 vcc, s2, v50
	v_add_u32_e32 v50, 0x3c0, v184
	s_nop 0
	v_cndmask_b32_e32 v33, 0, v35, vcc
	v_and_b32_e32 v35, 0x7fffffff, v36
	v_pk_add_f32 v[34:35], v[34:35], 0 neg_lo:[1,1] neg_hi:[1,1]
	v_cmp_gt_i32_e32 vcc, 0, v37
	s_nop 1
	v_cndmask_b32_e32 v37, v34, v53, vcc
	v_cmp_gt_i32_e32 vcc, 0, v36
	s_waitcnt lgkmcnt(7)
	v_and_b32_e32 v36, 0x7fffffff, v39
	v_xor_b32_e32 v53, -1, v39
	v_cndmask_b32_e32 v34, v35, v52, vcc
	v_cmp_ge_i32_e32 vcc, s2, v51
	v_add_u32_e32 v51, 0x400, v184
	v_xor_b32_e32 v52, -1, v38
	v_cndmask_b32_e32 v34, 0, v34, vcc
	v_cmp_ge_i32_e32 vcc, s2, v50
	v_add_u32_e32 v50, 0x440, v184
	s_nop 0
	v_cndmask_b32_e32 v35, 0, v37, vcc
	v_and_b32_e32 v37, 0x7fffffff, v38
	v_pk_add_f32 v[36:37], v[36:37], 0 neg_lo:[1,1] neg_hi:[1,1]
	v_cmp_gt_i32_e32 vcc, 0, v39
	s_nop 1
	v_cndmask_b32_e32 v39, v36, v53, vcc
	v_cmp_gt_i32_e32 vcc, 0, v38
	s_waitcnt lgkmcnt(6)
; __device__ __forceinline__ unsigned fkey(float f) { const unsigned u = __builtin_bit_cast(unsigned, f); return (u & 0x80000000u) ? ~u : (u | 0x80000000u); }
; __device__ __forceinline__ void select_row(Frame& F, int row, int lane_, const LAS float* srl) {
;     ...
;             for (int j = 0; j < 32; ++j) { const int s = 64 * j + lane; const unsigned fk = fkey(sv[j]); key[j] = (s <= t) ? fk : 0u; }
;         }
;         unsigned long long* mr = F.MASK + (size_t)row * 32;
;         if (t + 1 <= TOPK) {
;             unsigned long long mine = 0ull;
; #pragma unroll
;             for (int j = 0; j < 32; ++j) { const unsigned long long bm = __ballot(key[j] != 0u); mine = (lane == j) ? bm : mine; }
;             if (lane < 32) mr[lane] = mine;
;             return;
;         }
;         unsigned T = 0u; bool exact = false;
;         const int nj = __builtin_amdgcn_readfirstlane((t + 64) >> 6);
;         int clo = t + 1, chi = 0, bit = 31;
;     ...
;             if (clo - chi <= 64) break;
;             const unsigned cand = T | (1u << bit);
;             int c = cnt_ge<0, 8>(key, cand);
;             if (nj > 8) { c += cnt_ge<8, 16>(key, cand); if (nj > 16) { c += cnt_ge<16, 24>(key, cand); if (nj > 24) c += cnt_ge<24, 32>(key, cand); } }
	v_and_b32_e32 v38, 0x7fffffff, v41
	v_xor_b32_e32 v53, -1, v41
	v_cndmask_b32_e32 v36, v37, v52, vcc
	v_cmp_ge_i32_e32 vcc, s2, v51
	v_add_u32_e32 v51, 0x480, v184
	v_xor_b32_e32 v52, -1, v40
	v_cndmask_b32_e32 v36, 0, v36, vcc
	v_cmp_ge_i32_e32 vcc, s2, v50
	v_add_u32_e32 v50, 0x4c0, v184
	s_nop 0
	v_cndmask_b32_e32 v37, 0, v39, vcc
	v_and_b32_e32 v39, 0x7fffffff, v40
	v_pk_add_f32 v[38:39], v[38:39], 0 neg_lo:[1,1] neg_hi:[1,1]
	v_cmp_gt_i32_e32 vcc, 0, v41
	s_nop 1
	v_cndmask_b32_e32 v41, v38, v53, vcc
	v_cmp_gt_i32_e32 vcc, 0, v40
	s_waitcnt lgkmcnt(5)
	v_and_b32_e32 v40, 0x7fffffff, v43
	v_xor_b32_e32 v53, -1, v43
	v_cndmask_b32_e32 v38, v39, v52, vcc
	v_cmp_ge_i32_e32 vcc, s2, v51
	v_add_u32_e32 v51, 0x500, v184
	v_xor_b32_e32 v52, -1, v42
	v_cndmask_b32_e32 v38, 0, v38, vcc
	v_cmp_ge_i32_e32 vcc, s2, v50
	v_add_u32_e32 v50, 0x540, v184
	s_nop 0
	v_cndmask_b32_e32 v39, 0, v41, vcc
	v_and_b32_e32 v41, 0x7fffffff, v42
	v_pk_add_f32 v[40:41], v[40:41], 0 neg_lo:[1,1] neg_hi:[1,1]
	v_cmp_gt_i32_e32 vcc, 0, v43
	s_nop 1
	v_cndmask_b32_e32 v43, v40, v53, vcc
	v_cmp_gt_i32_e32 vcc, 0, v42
	s_waitcnt lgkmcnt(4)
	v_and_b32_e32 v42, 0x7fffffff, v45
	v_xor_b32_e32 v53, -1, v45
	v_cndmask_b32_e32 v40, v41, v52, vcc
	v_cmp_ge_i32_e32 vcc, s2, v51
	v_add_u32_e32 v51, 0x580, v184
	v_xor_b32_e32 v52, -1, v44
	v_cndmask_b32_e32 v40, 0, v40, vcc
	v_cmp_ge_i32_e32 vcc, s2, v50
	v_add_u32_e32 v50, 0x5c0, v184
	s_nop 0
	v_cndmask_b32_e32 v41, 0, v43, vcc
	v_and_b32_e32 v43, 0x7fffffff, v44
	v_pk_add_f32 v[42:43], v[42:43], 0 neg_lo:[1,1] neg_hi:[1,1]
	v_cmp_gt_i32_e32 vcc, 0, v45
	s_nop 1
	v_cndmask_b32_e32 v45, v42, v53, vcc
	v_cmp_gt_i32_e32 vcc, 0, v44
	s_waitcnt lgkmcnt(3)
	v_and_b32_e32 v44, 0x7fffffff, v47
	v_xor_b32_e32 v53, -1, v47
	v_cndmask_b32_e32 v42, v43, v52, vcc
	v_cmp_ge_i32_e32 vcc, s2, v51
	v_add_u32_e32 v51, 0x600, v184
	v_xor_b32_e32 v52, -1, v46
	v_cndmask_b32_e32 v42, 0, v42, vcc
	v_cmp_ge_i32_e32 vcc, s2, v50
	v_add_u32_e32 v50, 0x640, v184
	s_nop 0
	v_cndmask_b32_e32 v43, 0, v45, vcc
	v_and_b32_e32 v45, 0x7fffffff, v46
	v_pk_add_f32 v[44:45], v[44:45], 0 neg_lo:[1,1] neg_hi:[1,1]
	v_cmp_gt_i32_e32 vcc, 0, v47
	s_nop 1
	v_cndmask_b32_e32 v47, v44, v53, vcc
	v_cmp_gt_i32_e32 vcc, 0, v46
	s_waitcnt lgkmcnt(2)
	v_and_b32_e32 v46, 0x7fffffff, v49
	v_xor_b32_e32 v53, -1, v49
	v_cndmask_b32_e32 v44, v45, v52, vcc
	v_cmp_ge_i32_e32 vcc, s2, v51
	v_add_u32_e32 v51, 0x680, v184
	v_xor_b32_e32 v52, -1, v48
	v_cndmask_b32_e32 v44, 0, v44, vcc
	v_cmp_ge_i32_e32 vcc, s2, v50
	v_add_u32_e32 v50, 0x6c0, v184
	s_nop 0
	v_cndmask_b32_e32 v45, 0, v47, vcc
	v_and_b32_e32 v47, 0x7fffffff, v48
	v_pk_add_f32 v[46:47], v[46:47], 0 neg_lo:[1,1] neg_hi:[1,1]
	v_cmp_gt_i32_e32 vcc, 0, v49
	s_nop 1
	v_cndmask_b32_e32 v49, v46, v53, vcc
	v_cmp_gt_i32_e32 vcc, 0, v48
	s_waitcnt lgkmcnt(1)
	v_and_b32_e32 v48, 0x7fffffff, v19
	v_xor_b32_e32 v53, -1, v19
	v_cndmask_b32_e32 v46, v47, v52, vcc
	v_cmp_ge_i32_e32 vcc, s2, v51
	v_add_u32_e32 v51, 0x700, v184
	v_xor_b32_e32 v52, -1, v18
	v_cndmask_b32_e32 v46, 0, v46, vcc
	v_cmp_ge_i32_e32 vcc, s2, v50
	v_add_u32_e32 v50, 0x740, v184
	s_nop 0
	v_cndmask_b32_e32 v47, 0, v49, vcc
	v_and_b32_e32 v49, 0x7fffffff, v18
	v_pk_add_f32 v[48:49], v[48:49], 0 neg_lo:[1,1] neg_hi:[1,1]
	v_cmp_gt_i32_e32 vcc, 0, v19
	s_nop 1
	v_cndmask_b32_e32 v19, v48, v53, vcc
	v_cmp_gt_i32_e32 vcc, 0, v18
	s_waitcnt lgkmcnt(0)
	v_and_b32_e32 v48, 0x7fffffff, v17
	v_xor_b32_e32 v53, -1, v17
	v_cndmask_b32_e32 v18, v49, v52, vcc
	v_cmp_ge_i32_e32 vcc, s2, v51
	v_and_b32_e32 v49, 0x7fffffff, v16
	v_pk_add_f32 v[48:49], v[48:49], 0 neg_lo:[1,1] neg_hi:[1,1]
	v_cndmask_b32_e32 v18, 0, v18, vcc
	v_cmp_ge_i32_e32 vcc, s2, v50
	v_add_u32_e32 v51, 0x780, v184
	v_xor_b32_e32 v52, -1, v16
	v_cndmask_b32_e32 v19, 0, v19, vcc
	v_cmp_gt_i32_e32 vcc, 0, v17
	v_add_u32_e32 v50, 0x7c0, v184
	s_nop 0
	v_cndmask_b32_e32 v17, v48, v53, vcc
	v_cmp_gt_i32_e32 vcc, 0, v16
	s_nop 1
	v_cndmask_b32_e32 v16, v49, v52, vcc
	v_cmp_ge_i32_e32 vcc, s2, v51
	s_nop 1
	v_cndmask_b32_e32 v48, 0, v16, vcc
	v_cmp_ge_i32_e32 vcc, s2, v50
	s_nop 1
	v_cndmask_b32_e32 v49, 0, v17, vcc
	s_cbranch_scc0 .LBB0_393
	s_add_i32 s23, s2, 1
	s_cmpk_gt_u32 s2, 0x1ff
	s_cselect_b64 s[4:5], -1, 0
	s_cmpk_gt_u32 s2, 0x3ff
	v_writelane_b32 v255, s0, 47
	s_cselect_b64 s[16:17], -1, 0
	s_cmpk_gt_u32 s2, 0x5ff
	v_writelane_b32 v255, s1, 48
	s_cselect_b64 s[68:69], -1, 0
	s_mov_b32 s18, 31
	s_mov_b64 s[2:3], 0
	s_mov_b32 s20, 0
	s_mov_b32 s13, 0
	v_max3_u32 v16, v20, v21, v22
	v_max3_u32 v16, v16, v23, v24
	v_max3_u32 v16, v16, v25, v26
	v_max3_u32 v16, v16, v27, v28
	v_max3_u32 v16, v16, v29, v30
	v_max3_u32 v16, v16, v31, v32
	v_max3_u32 v16, v16, v33, v34
	v_max3_u32 v16, v16, v35, v36
	v_max3_u32 v16, v16, v37, v38
	v_max3_u32 v16, v16, v39, v40
	v_max3_u32 v16, v16, v41, v42
	v_max3_u32 v16, v16, v43, v44
	v_max3_u32 v16, v16, v45, v46
	v_max3_u32 v16, v16, v47, v18
	v_max3_u32 v16, v16, v19, v48
	v_max_u32_e32 v16, v16, v49
	s_nop 1
	v_max_u32_dpp v16, v16, v16 quad_perm:[1,0,3,2] row_mask:0xf bank_mask:0xf
	s_nop 1
	v_max_u32_dpp v16, v16, v16 quad_perm:[2,3,0,1] row_mask:0xf bank_mask:0xf
	s_nop 1
	v_max_u32_dpp v16, v16, v16 row_half_mirror row_mask:0xf bank_mask:0xf
	s_nop 1
	v_max_u32_dpp v16, v16, v16 row_mirror row_mask:0xf bank_mask:0xf
	s_nop 1
	v_readlane_b32 s0, v16, 0
	v_readlane_b32 s1, v16, 16
	v_readlane_b32 s6, v16, 32
	v_readlane_b32 s7, v16, 48
	s_max_u32 s0, s0, s1
	s_max_u32 s6, s6, s7
	s_max_u32 s101, s0, s6
; template <int J0, int J1> __device__ __forceinline__ int cnt_ge(const unsigned (&key)[32], unsigned cand) {
;     int c = 0;
; #pragma unroll
;     for (int j = J0; j < J1; ++j) c += __popcll(__ballot(key[j] >= cand));
;     return c;
; }
; __device__ __forceinline__ void select_row(Frame& F, int row, int lane_, const LAS float* srl) {
;     ...
;             if (clo - chi <= 64) break;
;             const unsigned cand = T | (1u << bit);
;             int c = cnt_ge<0, 8>(key, cand);
;             if (nj > 8) { c += cnt_ge<8, 16>(key, cand); if (nj > 16) { c += cnt_ge<16, 24>(key, cand); if (nj > 24) c += cnt_ge<24, 32>(key, cand); } }
;             if (c >= TOPK) { T = cand; clo = c; if (c == TOPK) { exact = true; break; } } else chi = c;
.LBB0_381:
	s_lshl_b32 s0, 1, s18
	s_or_b32 s22, s0, s20
	s_cmp_gt_u32 s22, s101
	s_cbranch_scc1 .Lsel2_none
	v_cmp_le_u32_e64 s[44:45], s22, v20
	v_cmp_le_u32_e64 s[46:47], s22, v21
	v_cmp_le_u32_e64 s[48:49], s22, v22
	v_cmp_le_u32_e64 s[50:51], s22, v23
	s_bcnt1_i32_b64 s0, s[44:45]
	v_cmp_le_u32_e64 s[44:45], s22, v24
	s_bcnt1_i32_b64 s1, s[46:47]
	v_cmp_le_u32_e64 s[46:47], s22, v25
	s_add_i32 s0, s0, s1
	s_bcnt1_i32_b64 s1, s[48:49]
	v_cmp_le_u32_e64 s[48:49], s22, v26
	s_add_i32 s0, s0, s1
	s_bcnt1_i32_b64 s1, s[50:51]
	v_cmp_le_u32_e64 s[50:51], s22, v27
	s_add_i32 s0, s0, s1
	s_bcnt1_i32_b64 s1, s[44:45]
	s_add_i32 s0, s0, s1
	s_bcnt1_i32_b64 s1, s[46:47]
	s_add_i32 s0, s0, s1
	s_bcnt1_i32_b64 s1, s[48:49]
	s_add_i32 s0, s0, s1
	s_bcnt1_i32_b64 s1, s[50:51]
	s_add_i32 s38, s0, s1
	v_cndmask_b32_e64 v16, 0, 1, s[4:5]
	v_cmp_ne_u32_e64 s[36:37], 1, v16
	s_andn2_b64 vcc, exec, s[4:5]
	s_cbranch_vccnz .LBB0_385
	v_cmp_le_u32_e64 s[44:45], s22, v28
	v_cmp_le_u32_e64 s[46:47], s22, v29
	v_cmp_le_u32_e64 s[48:49], s22, v30
	v_cmp_le_u32_e64 s[50:51], s22, v31
	s_bcnt1_i32_b64 s1, s[44:45]
	v_cmp_le_u32_e64 s[44:45], s22, v32
	s_add_i32 s0, s38, s1
	s_bcnt1_i32_b64 s1, s[46:47]
	v_cmp_le_u32_e64 s[46:47], s22, v33
	s_add_i32 s0, s0, s1
	s_bcnt1_i32_b64 s1, s[48:49]
	v_cmp_le_u32_e64 s[48:49], s22, v34
	s_add_i32 s0, s0, s1
	s_bcnt1_i32_b64 s1, s[50:51]
	v_cmp_le_u32_e64 s[50:51], s22, v35
	s_add_i32 s0, s0, s1
	s_bcnt1_i32_b64 s1, s[44:45]
	s_add_i32 s0, s0, s1
	s_bcnt1_i32_b64 s1, s[46:47]
	s_add_i32 s0, s0, s1
	s_bcnt1_i32_b64 s1, s[48:49]
	s_add_i32 s0, s0, s1
	s_bcnt1_i32_b64 s1, s[50:51]
	s_add_i32 s38, s0, s1
	s_andn2_b64 vcc, exec, s[16:17]
	s_cbranch_vccnz .LBB0_385
	v_cmp_le_u32_e64 s[44:45], s22, v36
	v_cmp_le_u32_e64 s[46:47], s22, v37
	v_cmp_le_u32_e64 s[48:49], s22, v38
	v_cmp_le_u32_e64 s[50:51], s22, v39
	s_bcnt1_i32_b64 s1, s[44:45]
	v_cmp_le_u32_e64 s[44:45], s22, v40
	s_add_i32 s0, s38, s1
	s_bcnt1_i32_b64 s1, s[46:47]
	v_cmp_le_u32_e64 s[46:47], s22, v41
	s_add_i32 s0, s0, s1
	s_bcnt1_i32_b64 s1, s[48:49]
	v_cmp_le_u32_e64 s[48:49], s22, v42
	s_add_i32 s0, s0, s1
	s_bcnt1_i32_b64 s1, s[50:51]
	v_cmp_le_u32_e64 s[50:51], s22, v43
	s_add_i32 s0, s0, s1
	s_bcnt1_i32_b64 s1, s[44:45]
	s_add_i32 s0, s0, s1
	s_bcnt1_i32_b64 s1, s[46:47]
	s_add_i32 s0, s0, s1
	s_bcnt1_i32_b64 s1, s[48:49]
	s_add_i32 s0, s0, s1
	s_bcnt1_i32_b64 s1, s[50:51]
	s_add_i32 s38, s0, s1
	s_andn2_b64 vcc, exec, s[68:69]
	s_cbranch_vccnz .LBB0_385
	v_cmp_le_u32_e64 s[44:45], s22, v44
	v_cmp_le_u32_e64 s[46:47], s22, v45
	v_cmp_le_u32_e64 s[48:49], s22, v46
	v_cmp_le_u32_e64 s[50:51], s22, v47
	s_bcnt1_i32_b64 s1, s[44:45]
	v_cmp_le_u32_e64 s[44:45], s22, v18
	s_add_i32 s0, s38, s1
	s_bcnt1_i32_b64 s1, s[46:47]
	v_cmp_le_u32_e64 s[46:47], s22, v19
	s_add_i32 s0, s0, s1
	s_bcnt1_i32_b64 s1, s[48:49]
	v_cmp_le_u32_e64 s[48:49], s22, v48
	s_add_i32 s0, s0, s1
	s_bcnt1_i32_b64 s1, s[50:51]
	v_cmp_le_u32_e64 s[50:51], s22, v49
	s_add_i32 s0, s0, s1
	s_bcnt1_i32_b64 s1, s[44:45]
	s_add_i32 s0, s0, s1
	s_bcnt1_i32_b64 s1, s[46:47]
	s_add_i32 s0, s0, s1
	s_bcnt1_i32_b64 s1, s[48:49]
	s_add_i32 s0, s0, s1
	s_bcnt1_i32_b64 s1, s[50:51]
	s_add_i32 s38, s0, s1
